# attention unit prologue: rope-table and second-map Q loads hoisted next to the first load batch (one exposed memory round trip instead of four to six), both GQA and differential paths
# baseline (speedup 1.0000x reference)
.LBB0_623:
	s_or_b64 exec, exec, s[46:47]
	v_mov_b32_e32 v0, s44
	s_waitcnt lgkmcnt(0)
	s_barrier
	ds_read_b32 v0, v0
	s_mul_i32 s4, s96, 12
	s_mov_b64 s[46:47], -1
	s_waitcnt lgkmcnt(0)
	v_cmp_le_i32_e32 vcc, s4, v0
	v_readfirstlane_b32 s2, v0
	s_cbranch_vccnz .LBB0_618
	s_cmp_ge_i32 s2, s97
	v_lshlrev_b32_e32 v112, 1, v170
	s_cbranch_scc0 .LBB0_634
	s_sub_i32 s4, s2, s97
	s_mul_hi_u32 s12, s4, s25
	s_mul_i32 s13, s12, s96
	s_sub_i32 s13, s4, s13
	s_add_i32 s14, s12, 1
	s_sub_i32 s28, s13, s96
	s_cmp_ge_u32 s13, s96
	s_cselect_b32 s12, s14, s12
	s_cselect_b32 s13, s28, s13
	s_add_i32 s14, s12, 1
	s_cmp_ge_u32 s13, s96
	s_cselect_b32 s12, s14, s12
	s_mul_i32 s13, s12, s96
	s_sub_i32 s4, s4, s13
	s_add_i32 s13, s12, s27
	s_lshr_b32 s13, s13, 1
	s_and_b32 s14, s12, 1
	s_add_i32 s28, s4, 1
	s_cmp_lt_i32 s4, 16
	s_cselect_b32 s28, s28, 0
	s_ashr_i32 s29, s28, 31
	s_cmp_eq_u32 s28, 0
	s_mul_i32 s4, s13, 0x1100
	s_cselect_b64 s[72:73], -1, 0
	s_lshl_b32 s70, s14, 7
	v_lshl_add_u32 v8, s28, 8, v216
	s_lshl_b64 s[28:29], s[28:29], 17
	v_lshl_add_u64 v[0:1], s[4:5], 0, v[168:169]
	v_cndmask_b32_e64 v41, v8, -1, s[72:73]
	v_lshl_add_u64 v[8:9], v[172:173], 0, s[4:5]
	s_add_u32 s28, s33, s28
	v_lshlrev_b64 v[0:1], 9, v[0:1]
	v_lshlrev_b64 v[8:9], 9, v[8:9]
	s_addc_u32 s29, s34, s29
	v_cmp_lt_i32_e32 vcc, -1, v41
	v_lshrrev_b32_e32 v40, 2, v41
	v_lshlrev_b32_e32 v41, 4, v41
	v_lshl_add_u64 v[0:1], s[90:91], 0, v[0:1]
	s_mov_b32 s71, s5
	v_lshl_add_u64 v[8:9], s[28:29], 0, v[8:9]
	s_lshl_b32 s4, s14, 8
	v_and_b32_e32 v40, 0x1ffffff0, v40
	v_and_b32_e32 v41, 0x3f0, v41
	v_lshl_add_u64 v[0:1], v[0:1], 0, s[70:71]
	v_lshl_add_u64 v[192:193], v[8:9], 0, s[4:5]
	v_add_u32_e32 v40, v40, v174
	v_add_u32_e32 v42, v41, v174
	v_readlane_b32 s28, v253, 28
	v_lshl_add_u64 v[0:1], v[0:1], 0, v[112:113]
	v_lshl_add_u64 v[80:81], v[174:175], 1, v[192:193]
	v_ashrrev_i32_e32 v41, 31, v40
	v_readlane_b32 s29, v253, 29
	v_ashrrev_i32_e32 v43, 31, v42
	global_load_dwordx4 v[4:7], v[0:1], off
	s_nop 0
	global_load_dwordx4 v[0:3], v[0:1], off offset:256
	s_nop 0
	global_load_dwordx4 v[32:35], v[176:177], off
	global_load_dwordx4 v[36:39], v[176:177], off offset:16
	global_load_dwordx4 v[24:27], v[176:177], off offset:64
	global_load_dwordx4 v[28:31], v[176:177], off offset:80
	global_load_dwordx4 v[16:19], v[176:177], off offset:128
	global_load_dwordx4 v[20:23], v[176:177], off offset:144
	global_load_dwordx4 v[8:11], v[176:177], off offset:192
	global_load_dwordx4 v[12:15], v[176:177], off offset:208
	v_lshl_add_u64 v[50:51], v[40:41], 3, s[28:29]
	v_lshl_add_u64 v[48:49], v[42:43], 3, s[28:29]
	global_load_dwordx4 v[44:47], v[80:81], off
	global_load_dwordx4 v[40:43], v[80:81], off offset:32
	global_load_dwordx4 v[56:59], v[80:81], off offset:64
	global_load_dwordx4 v[66:69], v[80:81], off offset:96
	global_load_dwordx4 v[150:153], v[80:81], off offset:128
	global_load_dwordx4 v[154:157], v[80:81], off offset:160
	global_load_dwordx4 v[158:161], v[80:81], off offset:192
	global_load_dwordx4 v[162:165], v[80:81], off offset:224
	s_and_saveexec_b64 s[98:99], vcc
	global_load_dwordx4 v[118:121], v[50:51], off offset:48
	global_load_dwordx4 v[122:125], v[50:51], off offset:32
	global_load_dwordx4 v[126:129], v[50:51], off offset:16
	global_load_dwordx4 v[130:133], v[50:51], off
	global_load_dwordx4 v[134:137], v[48:49], off offset:48
	global_load_dwordx4 v[138:141], v[48:49], off offset:32
	global_load_dwordx4 v[142:145], v[48:49], off offset:16
	global_load_dwordx4 v[146:149], v[48:49], off
	s_mov_b64 exec, s[98:99]
	s_waitcnt vmcnt(0)
	v_and_b32_e32 v53, 0xffff0000, v47
	v_lshlrev_b32_e32 v52, 16, v47
	s_waitcnt vmcnt(1)
	v_and_b32_e32 v73, 0xffff0000, v57
	s_waitcnt vmcnt(0)
	v_and_b32_e32 v65, 0xffff0000, v69
	v_lshlrev_b32_e32 v64, 16, v69
	v_and_b32_e32 v83, 0xffff0000, v68
	v_lshlrev_b32_e32 v82, 16, v68
	v_lshlrev_b32_e32 v72, 16, v57
	v_and_b32_e32 v69, 0xffff0000, v56
	v_lshlrev_b32_e32 v68, 16, v56
	v_and_b32_e32 v57, 0xffff0000, v45
	v_lshlrev_b32_e32 v56, 16, v45
	v_and_b32_e32 v45, 0xffff0000, v44
	v_and_b32_e32 v87, 0xffff0000, v66
	v_lshlrev_b32_e32 v86, 16, v66
	v_lshlrev_b32_e32 v44, 16, v44
	v_mul_f32_e32 v66, v45, v45
	v_and_b32_e32 v85, 0xffff0000, v67
	v_lshlrev_b32_e32 v84, 16, v67
	v_pk_fma_f32 v[66:67], v[44:45], v[44:45], v[66:67] op_sel_hi:[1,1,0]
	v_mul_f32_e32 v70, v57, v57
	v_pk_fma_f32 v[66:67], v[56:57], v[56:57], v[66:67]
	v_and_b32_e32 v47, 0xffff0000, v46
	v_lshlrev_b32_e32 v46, 16, v46
	v_pk_add_f32 v[66:67], v[70:71], v[66:67] op_sel_hi:[0,1]
	v_pk_fma_f32 v[66:67], v[46:47], v[46:47], v[66:67]
	v_mul_f32_e32 v70, v47, v47
	v_pk_add_f32 v[66:67], v[70:71], v[66:67] op_sel_hi:[0,1]
	v_pk_fma_f32 v[66:67], v[52:53], v[52:53], v[66:67]
	v_mul_f32_e32 v70, v53, v53
	v_and_b32_e32 v61, 0xffff0000, v41
	v_lshlrev_b32_e32 v60, 16, v41
	v_and_b32_e32 v41, 0xffff0000, v40
	v_lshlrev_b32_e32 v40, 16, v40
	v_pk_add_f32 v[66:67], v[70:71], v[66:67] op_sel_hi:[0,1]
	v_pk_fma_f32 v[66:67], v[40:41], v[40:41], v[66:67]
	v_mul_f32_e32 v70, v41, v41
	v_pk_add_f32 v[66:67], v[70:71], v[66:67] op_sel_hi:[0,1]
	v_pk_fma_f32 v[66:67], v[60:61], v[60:61], v[66:67]
	v_mul_f32_e32 v70, v61, v61
	v_and_b32_e32 v55, 0xffff0000, v59
	v_lshlrev_b32_e32 v54, 16, v59
	v_and_b32_e32 v63, 0xffff0000, v58
	v_lshlrev_b32_e32 v62, 16, v58
	v_and_b32_e32 v59, 0xffff0000, v43
	v_lshlrev_b32_e32 v58, 16, v43
	v_and_b32_e32 v43, 0xffff0000, v42
	v_lshlrev_b32_e32 v42, 16, v42
	v_pk_add_f32 v[66:67], v[70:71], v[66:67] op_sel_hi:[0,1]
	v_pk_fma_f32 v[66:67], v[42:43], v[42:43], v[66:67]
	v_mul_f32_e32 v70, v43, v43
	v_pk_add_f32 v[66:67], v[70:71], v[66:67] op_sel_hi:[0,1]
	v_pk_fma_f32 v[66:67], v[58:59], v[58:59], v[66:67]
	v_mul_f32_e32 v70, v59, v59
	v_pk_add_f32 v[66:67], v[70:71], v[66:67] op_sel_hi:[0,1]
	v_pk_fma_f32 v[66:67], v[68:69], v[68:69], v[66:67]
	v_mul_f32_e32 v70, v69, v69
	v_pk_add_f32 v[66:67], v[70:71], v[66:67] op_sel_hi:[0,1]
	v_pk_fma_f32 v[66:67], v[72:73], v[72:73], v[66:67]
	v_mul_f32_e32 v70, v73, v73
	v_pk_add_f32 v[66:67], v[70:71], v[66:67] op_sel_hi:[0,1]
	v_pk_fma_f32 v[66:67], v[62:63], v[62:63], v[66:67]
	v_mul_f32_e32 v70, v63, v63
	v_pk_add_f32 v[66:67], v[70:71], v[66:67] op_sel_hi:[0,1]
	v_pk_fma_f32 v[66:67], v[54:55], v[54:55], v[66:67]
	v_mul_f32_e32 v70, v55, v55
	v_pk_add_f32 v[66:67], v[70:71], v[66:67] op_sel_hi:[0,1]
	v_pk_fma_f32 v[66:67], v[86:87], v[86:87], v[66:67]
	v_mul_f32_e32 v70, v87, v87
	v_pk_add_f32 v[66:67], v[70:71], v[66:67] op_sel_hi:[0,1]
	v_pk_fma_f32 v[66:67], v[84:85], v[84:85], v[66:67]
	v_mul_f32_e32 v70, v85, v85
	v_pk_add_f32 v[66:67], v[70:71], v[66:67] op_sel_hi:[0,1]
	v_pk_fma_f32 v[66:67], v[82:83], v[82:83], v[66:67]
	v_mul_f32_e32 v70, v83, v83
	v_pk_add_f32 v[66:67], v[70:71], v[66:67] op_sel_hi:[0,1]
	v_pk_fma_f32 v[66:67], v[64:65], v[64:65], v[66:67]
	v_mul_f32_e32 v70, v65, v65
	v_pk_add_f32 v[66:67], v[70:71], v[66:67] op_sel_hi:[0,1]
	v_mov_b32_e32 v67, v66
	s_nop 1
	v_permlane32_swap_b32_e32 v66, v67
	v_add_f32_e32 v66, v66, v67
	v_fmamk_f32 v66, v66, 0x3c800000, v196
	v_cmp_gt_f32_e64 s[46:47], s35, v66
	v_mul_f32_e32 v67, 0x4b800000, v66
	s_nop 0
	v_cndmask_b32_e64 v66, v66, v67, s[46:47]
	v_rsq_f32_e32 v66, v66
	s_nop 0
	v_mul_f32_e32 v67, 0x45800000, v66
	v_cndmask_b32_e64 v88, v66, v67, s[46:47]
	v_pk_mul_f32 v[66:67], v[32:33], v[88:89] op_sel_hi:[1,0]
	v_pk_mul_f32 v[70:71], v[36:37], v[88:89] op_sel_hi:[1,0]
	v_pk_mul_f32 v[78:79], v[66:67], v[44:45]
	v_pk_mul_f32 v[70:71], v[70:71], v[46:47]
	v_pk_mul_f32 v[44:45], v[34:35], v[88:89] op_sel_hi:[1,0]
	v_pk_mul_f32 v[46:47], v[38:39], v[88:89] op_sel_hi:[1,0]
	v_pk_mul_f32 v[74:75], v[44:45], v[56:57]
	v_pk_mul_f32 v[66:67], v[46:47], v[52:53]
	v_pk_mul_f32 v[44:45], v[24:25], v[88:89] op_sel_hi:[1,0]
	v_pk_mul_f32 v[46:47], v[28:29], v[88:89] op_sel_hi:[1,0]
	v_pk_mul_f32 v[56:57], v[44:45], v[40:41]
	v_pk_mul_f32 v[52:53], v[46:47], v[42:43]
	v_pk_mul_f32 v[40:41], v[26:27], v[88:89] op_sel_hi:[1,0]
	v_pk_mul_f32 v[42:43], v[30:31], v[88:89] op_sel_hi:[1,0]
	v_pk_mul_f32 v[60:61], v[40:41], v[60:61]
	v_pk_mul_f32 v[58:59], v[42:43], v[58:59]
	v_pk_mul_f32 v[40:41], v[16:17], v[88:89] op_sel_hi:[1,0]
	v_pk_mul_f32 v[42:43], v[20:21], v[88:89] op_sel_hi:[1,0]
	v_pk_mul_f32 v[76:77], v[40:41], v[68:69]
	v_pk_mul_f32 v[68:69], v[42:43], v[62:63]
	v_pk_mul_f32 v[40:41], v[18:19], v[88:89] op_sel_hi:[1,0]
	v_pk_mul_f32 v[42:43], v[22:23], v[88:89] op_sel_hi:[1,0]
	v_pk_mul_f32 v[72:73], v[40:41], v[72:73]
	v_pk_mul_f32 v[62:63], v[42:43], v[54:55]
	v_pk_mul_f32 v[40:41], v[8:9], v[88:89] op_sel_hi:[1,0]
	v_pk_mul_f32 v[42:43], v[12:13], v[88:89] op_sel_hi:[1,0]
	v_pk_mul_f32 v[46:47], v[40:41], v[86:87]
	v_pk_mul_f32 v[44:45], v[42:43], v[82:83]
	v_pk_mul_f32 v[40:41], v[10:11], v[88:89] op_sel_hi:[1,0]
	v_pk_mul_f32 v[42:43], v[14:15], v[88:89] op_sel_hi:[1,0]
	v_pk_mul_f32 v[54:55], v[40:41], v[84:85]
	v_pk_mul_f32 v[64:65], v[42:43], v[64:65]
	s_and_saveexec_b64 s[46:47], vcc
	s_cbranch_execz .LBB0_627
	v_mov_b64_e32 v[86:87], v[118:119]
	v_mov_b64_e32 v[88:89], v[120:121]
	v_mov_b64_e32 v[90:91], v[122:123]
	v_mov_b64_e32 v[92:93], v[124:125]
	v_mov_b64_e32 v[94:95], v[126:127]
	v_mov_b64_e32 v[96:97], v[128:129]
	v_mov_b64_e32 v[82:83], v[130:131]
	v_mov_b64_e32 v[84:85], v[132:133]
	v_mov_b64_e32 v[40:41], v[134:135]
	v_mov_b64_e32 v[42:43], v[136:137]
	v_mov_b64_e32 v[98:99], v[138:139]
	v_mov_b64_e32 v[100:101], v[140:141]
	v_mov_b64_e32 v[102:103], v[142:143]
	v_mov_b64_e32 v[104:105], v[144:145]
	v_mov_b64_e32 v[106:107], v[146:147]
	v_mov_b64_e32 v[108:109], v[148:149]
	s_waitcnt vmcnt(4)
	v_mov_b32_e32 v110, v82
	v_mov_b32_e32 v111, v84
	v_mov_b32_e32 v84, v83
	v_pk_mul_f32 v[82:83], v[56:57], v[84:85]
	v_pk_mul_f32 v[56:57], v[56:57], v[110:111]
	v_pk_fma_f32 v[82:83], v[78:79], v[110:111], v[82:83] neg_lo:[0,0,1] neg_hi:[0,0,1]
	v_pk_fma_f32 v[56:57], v[78:79], v[84:85], v[56:57]
	s_waitcnt vmcnt(0)
	v_mov_b32_e32 v84, v106
	v_mov_b32_e32 v85, v108
	v_mov_b32_e32 v108, v107
	v_pk_mul_f32 v[78:79], v[46:47], v[108:109]
	v_pk_mul_f32 v[46:47], v[46:47], v[84:85]
	v_pk_fma_f32 v[78:79], v[76:77], v[84:85], v[78:79] neg_lo:[0,0,1] neg_hi:[0,0,1]
	v_pk_fma_f32 v[46:47], v[76:77], v[108:109], v[46:47]
	v_mov_b32_e32 v76, v94
	v_mov_b32_e32 v77, v96
	v_mov_b32_e32 v96, v95
	v_pk_mul_f32 v[84:85], v[60:61], v[96:97]
	v_pk_mul_f32 v[60:61], v[60:61], v[76:77]
	v_pk_fma_f32 v[84:85], v[74:75], v[76:77], v[84:85] neg_lo:[0,0,1] neg_hi:[0,0,1]
	v_pk_fma_f32 v[60:61], v[74:75], v[96:97], v[60:61]
	v_mov_b32_e32 v74, v102
	v_mov_b32_e32 v75, v104
	v_mov_b32_e32 v104, v103
	v_pk_mul_f32 v[76:77], v[54:55], v[104:105]
	v_pk_mul_f32 v[54:55], v[54:55], v[74:75]
	v_pk_fma_f32 v[76:77], v[72:73], v[74:75], v[76:77] neg_lo:[0,0,1] neg_hi:[0,0,1]
	v_pk_fma_f32 v[54:55], v[72:73], v[104:105], v[54:55]
	v_mov_b32_e32 v72, v90
	v_mov_b32_e32 v73, v92
	v_mov_b32_e32 v92, v91
	v_pk_mul_f32 v[74:75], v[52:53], v[92:93]
	v_pk_mul_f32 v[52:53], v[52:53], v[72:73]
	v_pk_fma_f32 v[74:75], v[70:71], v[72:73], v[74:75] neg_lo:[0,0,1] neg_hi:[0,0,1]
	v_pk_fma_f32 v[52:53], v[70:71], v[92:93], v[52:53]
	v_mov_b32_e32 v70, v98
	v_mov_b32_e32 v71, v100
	v_mov_b32_e32 v100, v99
	v_pk_mul_f32 v[72:73], v[44:45], v[100:101]
	v_pk_mul_f32 v[44:45], v[44:45], v[70:71]
	v_pk_fma_f32 v[72:73], v[68:69], v[70:71], v[72:73] neg_lo:[0,0,1] neg_hi:[0,0,1]
	v_pk_fma_f32 v[44:45], v[68:69], v[100:101], v[44:45]
	v_mov_b32_e32 v68, v86
	v_mov_b32_e32 v69, v88
	v_mov_b32_e32 v88, v87
	v_pk_mul_f32 v[70:71], v[58:59], v[88:89]
	v_pk_mul_f32 v[58:59], v[58:59], v[68:69]
	v_pk_fma_f32 v[70:71], v[66:67], v[68:69], v[70:71] neg_lo:[0,0,1] neg_hi:[0,0,1]
	v_pk_fma_f32 v[58:59], v[66:67], v[88:89], v[58:59]
	v_mov_b32_e32 v67, v42
	v_mov_b32_e32 v42, v41
	v_mov_b32_e32 v66, v40
	v_pk_mul_f32 v[40:41], v[64:65], v[42:43]
	v_pk_mul_f32 v[64:65], v[64:65], v[66:67]
	v_pk_fma_f32 v[40:41], v[62:63], v[66:67], v[40:41] neg_lo:[0,0,1] neg_hi:[0,0,1]
	v_pk_fma_f32 v[64:65], v[62:63], v[42:43], v[64:65]
	v_mov_b64_e32 v[62:63], v[40:41]
	v_mov_b64_e32 v[68:69], v[72:73]
	v_mov_b64_e32 v[72:73], v[76:77]
	v_mov_b64_e32 v[76:77], v[78:79]
	v_mov_b64_e32 v[66:67], v[70:71]
	v_mov_b64_e32 v[70:71], v[74:75]
	v_mov_b64_e32 v[74:75], v[84:85]
	v_mov_b64_e32 v[78:79], v[82:83]
.LBB0_627:
	s_or_b64 exec, exec, s[46:47]
	s_and_saveexec_b64 s[98:99], vcc
	global_load_dwordx4 v[118:121], v[50:51], off offset:48
	global_load_dwordx4 v[122:125], v[50:51], off offset:32
	global_load_dwordx4 v[126:129], v[50:51], off offset:16
	global_load_dwordx4 v[130:133], v[50:51], off
	global_load_dwordx4 v[134:137], v[48:49], off offset:48
	global_load_dwordx4 v[138:141], v[48:49], off offset:32
	global_load_dwordx4 v[142:145], v[48:49], off offset:16
	global_load_dwordx4 v[146:149], v[48:49], off
	s_mov_b64 exec, s[98:99]
	v_mov_b64_e32 v[100:101], v[150:151]
	v_mov_b64_e32 v[102:103], v[152:153]
	v_mov_b64_e32 v[108:109], v[154:155]
	v_mov_b64_e32 v[110:111], v[156:157]
	v_mov_b64_e32 v[84:85], v[158:159]
	v_mov_b64_e32 v[86:87], v[160:161]
	v_mov_b64_e32 v[92:93], v[162:163]
	v_mov_b64_e32 v[94:95], v[164:165]
	v_and_b32_e32 v107, 0xffff0000, v100
	v_and_b32_e32 v99, 0xffff0000, v103
	v_lshlrev_b32_e32 v98, 16, v103
	v_and_b32_e32 v105, 0xffff0000, v102
	v_lshlrev_b32_e32 v104, 16, v102
	v_and_b32_e32 v103, 0xffff0000, v101
	v_lshlrev_b32_e32 v102, 16, v101
	v_lshlrev_b32_e32 v106, 16, v100
	v_and_b32_e32 v101, 0xffff0000, v108
	v_lshlrev_b32_e32 v100, 16, v108
	v_mul_f32_e32 v108, v107, v107
	v_and_b32_e32 v41, 0xffff0000, v95
	v_lshlrev_b32_e32 v40, 16, v95
	v_and_b32_e32 v81, 0xffff0000, v94
	v_lshlrev_b32_e32 v80, 16, v94
	v_and_b32_e32 v95, 0xffff0000, v109
	v_lshlrev_b32_e32 v94, 16, v109
	v_pk_fma_f32 v[108:109], v[106:107], v[106:107], v[108:109] op_sel_hi:[1,1,0]
	v_and_b32_e32 v97, 0xffff0000, v110
	v_lshlrev_b32_e32 v96, 16, v110
	v_pk_fma_f32 v[108:109], v[102:103], v[102:103], v[108:109]
	v_mul_f32_e32 v110, v103, v103
	v_pk_add_f32 v[108:109], v[110:111], v[108:109] op_sel_hi:[0,1]
	v_pk_fma_f32 v[108:109], v[104:105], v[104:105], v[108:109]
	v_mul_f32_e32 v110, v105, v105
	v_pk_add_f32 v[108:109], v[110:111], v[108:109] op_sel_hi:[0,1]
	v_pk_fma_f32 v[108:109], v[98:99], v[98:99], v[108:109]
	v_mul_f32_e32 v110, v99, v99
	v_pk_add_f32 v[108:109], v[110:111], v[108:109] op_sel_hi:[0,1]
	v_pk_fma_f32 v[108:109], v[100:101], v[100:101], v[108:109]
	v_mul_f32_e32 v110, v101, v101
	v_pk_add_f32 v[108:109], v[110:111], v[108:109] op_sel_hi:[0,1]
	v_pk_fma_f32 v[108:109], v[94:95], v[94:95], v[108:109]
	v_mul_f32_e32 v110, v95, v95
	v_pk_add_f32 v[108:109], v[110:111], v[108:109] op_sel_hi:[0,1]
	v_pk_fma_f32 v[108:109], v[96:97], v[96:97], v[108:109]
	v_mul_f32_e32 v110, v97, v97
	v_and_b32_e32 v83, 0xffff0000, v87
	v_lshlrev_b32_e32 v82, 16, v87
	v_and_b32_e32 v89, 0xffff0000, v86
	v_lshlrev_b32_e32 v88, 16, v86
	v_and_b32_e32 v87, 0xffff0000, v85
	v_lshlrev_b32_e32 v86, 16, v85
	v_and_b32_e32 v43, 0xffff0000, v93
	v_lshlrev_b32_e32 v42, 16, v93
	v_and_b32_e32 v91, 0xffff0000, v84
	v_lshlrev_b32_e32 v90, 16, v84
	v_and_b32_e32 v85, 0xffff0000, v92
	v_lshlrev_b32_e32 v84, 16, v92
	v_and_b32_e32 v93, 0xffff0000, v111
	v_lshlrev_b32_e32 v92, 16, v111
	v_pk_add_f32 v[108:109], v[110:111], v[108:109] op_sel_hi:[0,1]
	v_pk_fma_f32 v[108:109], v[92:93], v[92:93], v[108:109]
	v_mul_f32_e32 v110, v93, v93
	v_pk_add_f32 v[108:109], v[110:111], v[108:109] op_sel_hi:[0,1]
	v_pk_fma_f32 v[108:109], v[90:91], v[90:91], v[108:109]
	v_mul_f32_e32 v110, v91, v91
	v_pk_add_f32 v[108:109], v[110:111], v[108:109] op_sel_hi:[0,1]
	v_pk_fma_f32 v[108:109], v[86:87], v[86:87], v[108:109]
	v_mul_f32_e32 v110, v87, v87
	v_pk_add_f32 v[108:109], v[110:111], v[108:109] op_sel_hi:[0,1]
	v_pk_fma_f32 v[108:109], v[88:89], v[88:89], v[108:109]
	v_mul_f32_e32 v110, v89, v89
	v_pk_add_f32 v[108:109], v[110:111], v[108:109] op_sel_hi:[0,1]
	v_pk_fma_f32 v[108:109], v[82:83], v[82:83], v[108:109]
	v_mul_f32_e32 v110, v83, v83
	v_pk_add_f32 v[108:109], v[110:111], v[108:109] op_sel_hi:[0,1]
	v_pk_fma_f32 v[108:109], v[84:85], v[84:85], v[108:109]
	v_mul_f32_e32 v110, v85, v85
	v_pk_add_f32 v[108:109], v[110:111], v[108:109] op_sel_hi:[0,1]
	v_pk_fma_f32 v[108:109], v[42:43], v[42:43], v[108:109]
	v_mul_f32_e32 v110, v43, v43
	v_pk_add_f32 v[108:109], v[110:111], v[108:109] op_sel_hi:[0,1]
	v_pk_fma_f32 v[108:109], v[80:81], v[80:81], v[108:109]
	v_mul_f32_e32 v110, v81, v81
	v_pk_add_f32 v[108:109], v[110:111], v[108:109] op_sel_hi:[0,1]
	v_pk_fma_f32 v[108:109], v[40:41], v[40:41], v[108:109]
	v_mul_f32_e32 v110, v41, v41
	v_pk_add_f32 v[108:109], v[110:111], v[108:109] op_sel_hi:[0,1]
	v_mov_b32_e32 v109, v108
	s_nop 1
	v_permlane32_swap_b32_e32 v108, v109
	v_add_f32_e32 v108, v108, v109
	v_fmamk_f32 v108, v108, 0x3c800000, v196
	v_cmp_gt_f32_e64 s[46:47], s35, v108
	v_mul_f32_e32 v109, 0x4b800000, v108
	s_nop 0
	v_cndmask_b32_e64 v108, v108, v109, s[46:47]
	v_rsq_f32_e32 v108, v108
	s_nop 0
	v_mul_f32_e32 v109, 0x45800000, v108
	v_cndmask_b32_e64 v108, v108, v109, s[46:47]
	v_pk_mul_f32 v[32:33], v[32:33], v[108:109] op_sel_hi:[1,0]
	v_pk_mul_f32 v[16:17], v[16:17], v[108:109] op_sel_hi:[1,0]
	v_pk_mul_f32 v[106:107], v[32:33], v[106:107]
	v_pk_mul_f32 v[32:33], v[34:35], v[108:109] op_sel_hi:[1,0]
	v_pk_mul_f32 v[34:35], v[38:39], v[108:109] op_sel_hi:[1,0]
	v_pk_mul_f32 v[102:103], v[32:33], v[102:103]
	v_pk_mul_f32 v[32:33], v[34:35], v[98:99]
	v_pk_mul_f32 v[24:25], v[24:25], v[108:109] op_sel_hi:[1,0]
	v_pk_mul_f32 v[34:35], v[28:29], v[108:109] op_sel_hi:[1,0]
	v_pk_mul_f32 v[90:91], v[16:17], v[90:91]
	v_pk_mul_f32 v[16:17], v[18:19], v[108:109] op_sel_hi:[1,0]
	v_pk_mul_f32 v[8:9], v[8:9], v[108:109] op_sel_hi:[1,0]
	v_pk_mul_f32 v[36:37], v[36:37], v[108:109] op_sel_hi:[1,0]
	v_pk_mul_f32 v[28:29], v[24:25], v[100:101]
	v_pk_mul_f32 v[24:25], v[34:35], v[96:97]
	v_pk_mul_f32 v[26:27], v[26:27], v[108:109] op_sel_hi:[1,0]
	v_pk_mul_f32 v[34:35], v[30:31], v[108:109] op_sel_hi:[1,0]
	v_pk_mul_f32 v[20:21], v[20:21], v[108:109] op_sel_hi:[1,0]
	v_pk_mul_f32 v[18:19], v[22:23], v[108:109] op_sel_hi:[1,0]
	v_pk_mul_f32 v[38:39], v[16:17], v[86:87]
	v_pk_mul_f32 v[12:13], v[12:13], v[108:109] op_sel_hi:[1,0]
	v_pk_mul_f32 v[16:17], v[8:9], v[84:85]
	v_pk_mul_f32 v[8:9], v[10:11], v[108:109] op_sel_hi:[1,0]
	v_pk_mul_f32 v[10:11], v[14:15], v[108:109] op_sel_hi:[1,0]
	v_pk_mul_f32 v[36:37], v[36:37], v[104:105]
	v_pk_mul_f32 v[30:31], v[26:27], v[94:95]
	v_pk_mul_f32 v[26:27], v[34:35], v[92:93]
	v_pk_mul_f32 v[34:35], v[20:21], v[88:89]
	v_pk_mul_f32 v[18:19], v[18:19], v[82:83]
	v_pk_mul_f32 v[12:13], v[12:13], v[80:81]
	v_pk_mul_f32 v[14:15], v[8:9], v[42:43]
	v_pk_mul_f32 v[20:21], v[10:11], v[40:41]
	s_and_saveexec_b64 s[46:47], vcc
	s_cbranch_execz .LBB0_629
	s_nop 0
	s_waitcnt vmcnt(0)
	v_mov_b64_e32 v[80:81], v[118:119]
	v_mov_b64_e32 v[82:83], v[120:121]
	v_mov_b64_e32 v[84:85], v[122:123]
	v_mov_b64_e32 v[86:87], v[124:125]
	v_mov_b64_e32 v[92:93], v[126:127]
	v_mov_b64_e32 v[94:95], v[128:129]
	v_mov_b64_e32 v[40:41], v[130:131]
	v_mov_b64_e32 v[42:43], v[132:133]
	v_mov_b64_e32 v[8:9], v[134:135]
	v_mov_b64_e32 v[10:11], v[136:137]
	v_mov_b64_e32 v[96:97], v[138:139]
	v_mov_b64_e32 v[98:99], v[140:141]
	v_mov_b64_e32 v[108:109], v[142:143]
	v_mov_b64_e32 v[110:111], v[144:145]
	v_mov_b64_e32 v[48:49], v[146:147]
	v_mov_b64_e32 v[50:51], v[148:149]
	v_mov_b32_e32 v88, v40
	v_mov_b32_e32 v89, v42
	v_mov_b32_e32 v42, v41
	v_pk_mul_f32 v[22:23], v[28:29], v[42:43]
	v_pk_mul_f32 v[28:29], v[28:29], v[88:89]
	v_pk_fma_f32 v[22:23], v[106:107], v[88:89], v[22:23] neg_lo:[0,0,1] neg_hi:[0,0,1]
	v_pk_fma_f32 v[28:29], v[106:107], v[42:43], v[28:29]
	s_waitcnt vmcnt(0)
	v_mov_b32_e32 v43, v50
	v_mov_b32_e32 v50, v49
	v_mov_b32_e32 v42, v48
	v_pk_mul_f32 v[40:41], v[16:17], v[50:51]
	v_mov_b32_e32 v49, v94
	v_mov_b32_e32 v94, v93
	v_pk_fma_f32 v[40:41], v[90:91], v[42:43], v[40:41] neg_lo:[0,0,1] neg_hi:[0,0,1]
	v_pk_mul_f32 v[16:17], v[16:17], v[42:43]
	v_mov_b32_e32 v48, v92
	v_pk_mul_f32 v[42:43], v[30:31], v[94:95]
	v_pk_mul_f32 v[30:31], v[30:31], v[48:49]
	v_pk_fma_f32 v[42:43], v[102:103], v[48:49], v[42:43] neg_lo:[0,0,1] neg_hi:[0,0,1]
	v_mov_b32_e32 v48, v108
	v_mov_b32_e32 v49, v110
	v_mov_b32_e32 v110, v109
	v_pk_fma_f32 v[16:17], v[90:91], v[50:51], v[16:17]
	v_pk_mul_f32 v[50:51], v[14:15], v[110:111]
	v_pk_mul_f32 v[14:15], v[14:15], v[48:49]
	v_pk_fma_f32 v[50:51], v[38:39], v[48:49], v[50:51] neg_lo:[0,0,1] neg_hi:[0,0,1]
	v_pk_fma_f32 v[14:15], v[38:39], v[110:111], v[14:15]
	v_mov_b32_e32 v38, v84
	v_mov_b32_e32 v39, v86
	v_mov_b32_e32 v86, v85
	v_pk_mul_f32 v[48:49], v[24:25], v[86:87]
	v_pk_mul_f32 v[24:25], v[24:25], v[38:39]
	v_pk_fma_f32 v[48:49], v[36:37], v[38:39], v[48:49] neg_lo:[0,0,1] neg_hi:[0,0,1]
	v_pk_fma_f32 v[24:25], v[36:37], v[86:87], v[24:25]
	v_mov_b32_e32 v36, v96
	v_mov_b32_e32 v37, v98
	v_mov_b32_e32 v98, v97
	v_pk_mul_f32 v[38:39], v[12:13], v[98:99]
	v_pk_mul_f32 v[12:13], v[12:13], v[36:37]
	v_pk_fma_f32 v[38:39], v[34:35], v[36:37], v[38:39] neg_lo:[0,0,1] neg_hi:[0,0,1]
	v_pk_fma_f32 v[12:13], v[34:35], v[98:99], v[12:13]
	v_mov_b32_e32 v34, v80
	v_mov_b32_e32 v35, v82
	v_mov_b32_e32 v82, v81
	v_pk_mul_f32 v[36:37], v[26:27], v[82:83]
	v_pk_mul_f32 v[26:27], v[26:27], v[34:35]
	v_pk_fma_f32 v[36:37], v[32:33], v[34:35], v[36:37] neg_lo:[0,0,1] neg_hi:[0,0,1]
	v_pk_fma_f32 v[26:27], v[32:33], v[82:83], v[26:27]
	v_mov_b32_e32 v33, v10
	v_mov_b32_e32 v10, v9
	v_mov_b32_e32 v32, v8
	v_pk_mul_f32 v[8:9], v[20:21], v[10:11]
	v_pk_mul_f32 v[20:21], v[20:21], v[32:33]
	v_pk_fma_f32 v[8:9], v[18:19], v[32:33], v[8:9] neg_lo:[0,0,1] neg_hi:[0,0,1]
	v_pk_fma_f32 v[30:31], v[102:103], v[94:95], v[30:31]
	v_pk_fma_f32 v[20:21], v[18:19], v[10:11], v[20:21]
	v_mov_b64_e32 v[18:19], v[8:9]
	v_mov_b64_e32 v[34:35], v[38:39]
	v_mov_b64_e32 v[38:39], v[50:51]
	v_mov_b64_e32 v[90:91], v[40:41]
	v_mov_b64_e32 v[32:33], v[36:37]
	v_mov_b64_e32 v[36:37], v[48:49]
	v_mov_b64_e32 v[102:103], v[42:43]
	v_mov_b64_e32 v[106:107], v[22:23]

.LBB0_634:
	s_and_b64 vcc, exec, s[46:47]
	s_cbranch_vccz .LBB0_617
	s_abs_i32 s12, s2
	s_mul_hi_u32 s13, s12, s25
	s_mul_i32 s14, s13, s96
	s_sub_i32 s12, s12, s14
	s_ashr_i32 s4, s2, 31
	s_add_i32 s14, s13, 1
	s_sub_i32 s28, s12, s96
	s_cmp_ge_u32 s12, s96
	s_cselect_b32 s13, s14, s13
	s_cselect_b32 s12, s28, s12
	s_add_i32 s14, s13, 1
	s_cmp_ge_u32 s12, s96
	s_cselect_b32 s12, s14, s13
	s_xor_b32 s12, s12, s4
	s_sub_i32 s12, s12, s4
	s_mul_i32 s4, s12, s96
	s_sub_i32 s4, s2, s4
	s_add_i32 s2, s12, s15
	s_ashr_i32 s2, s2, 2
	s_add_i32 s13, s4, 1
	s_cmp_lt_i32 s4, 16
	s_cselect_b32 s28, s13, 0
	s_ashr_i32 s29, s28, 31
	s_cmp_eq_u32 s28, 0
	s_cselect_b64 s[70:71], -1, 0
	s_lshl_b32 s4, s12, 7
	s_and_b32 s4, s4, 0x180
	v_lshl_add_u32 v8, s28, 8, v216
	s_lshl_b64 s[28:29], s[28:29], 17
	v_mad_i64_i32 v[0:1], s[36:37], s2, v204, v[168:169]
	v_cndmask_b32_e64 v24, v8, -1, s[70:71]
	v_mad_i64_i32 v[8:9], s[36:37], s2, v204, v[172:173]
	s_add_u32 s28, s16, s28
	v_lshlrev_b64 v[0:1], 9, v[0:1]
	v_lshlrev_b64 v[8:9], 9, v[8:9]
	s_addc_u32 s29, s17, s29
	v_lshl_add_u64 v[2:3], s[54:55], 0, v[0:1]
	v_lshl_add_u64 v[0:1], s[30:31], 0, v[0:1]
	v_lshl_add_u64 v[8:9], s[28:29], 0, v[8:9]
	v_lshl_add_u64 v[2:3], v[2:3], 0, s[4:5]
	v_lshl_add_u64 v[0:1], v[0:1], 0, s[4:5]
	v_lshl_add_u64 v[150:151], v[8:9], 0, s[4:5]
	v_lshl_add_u64 v[2:3], v[2:3], 0, v[112:113]
	v_lshl_add_u64 v[0:1], v[0:1], 0, v[112:113]
	v_lshl_add_u64 v[58:59], v[174:175], 1, v[150:151]
	global_load_dwordx4 v[4:7], v[2:3], off
	s_nop 0
	global_load_dwordx4 v[0:3], v[0:1], off
	s_nop 0
	global_load_dwordx4 v[16:19], v[184:185], off
	global_load_dwordx4 v[20:23], v[184:185], off offset:16
	global_load_dwordx4 v[8:11], v[184:185], off offset:64
	global_load_dwordx4 v[12:15], v[184:185], off offset:80
	global_load_dwordx4 v[28:31], v[58:59], off
	global_load_dwordx4 v[32:35], v[58:59], off offset:32
	v_and_b32_e32 v112, 0x7fffffc0, v24
	v_lshlrev_b32_e32 v25, 6, v24
	v_lshl_add_u64 v[56:57], s[52:53], 0, v[112:113]
	v_and_b32_e32 v112, 0xfc0, v25
	v_cmp_lt_i32_e32 vcc, -1, v24
	v_lshl_add_u64 v[54:55], s[52:53], 0, v[112:113]
	v_bitop3_b32 v112, v24, -8, 56 bitop3:0xc8
	v_lshl_add_u64 v[52:53], s[52:53], 0, v[112:113]
	global_load_dwordx4 v[152:155], v[58:59], off offset:64
	global_load_dwordx4 v[156:159], v[58:59], off offset:96
	s_and_saveexec_b64 s[98:99], vcc
	global_load_dwordx4 v[118:121], v[56:57], off offset:32
	global_load_dwordx4 v[122:125], v[56:57], off offset:16
	global_load_dwordx4 v[126:129], v[56:57], off
	global_load_dwordx2 v[130:131], v[56:57], off offset:48
	global_load_dwordx4 v[132:135], v[54:55], off offset:48
	global_load_dwordx4 v[136:139], v[54:55], off offset:32
	global_load_dwordx4 v[140:143], v[54:55], off offset:16
	global_load_dwordx4 v[144:147], v[54:55], off
	global_load_dwordx2 v[148:149], v[52:53], off
	s_mov_b64 exec, s[98:99]
	s_waitcnt vmcnt(0)
	v_and_b32_e32 v43, 0xffff0000, v29
	v_lshlrev_b32_e32 v42, 16, v29
	v_and_b32_e32 v29, 0xffff0000, v28
	v_lshlrev_b32_e32 v28, 16, v28
	v_mul_f32_e32 v36, v29, v29
	v_pk_fma_f32 v[36:37], v[28:29], v[28:29], v[36:37] op_sel_hi:[1,1,0]
	v_mul_f32_e32 v38, v43, v43
	v_pk_fma_f32 v[36:37], v[42:43], v[42:43], v[36:37]
	v_and_b32_e32 v41, 0xffff0000, v31
	v_lshlrev_b32_e32 v40, 16, v31
	v_and_b32_e32 v31, 0xffff0000, v30
	v_lshlrev_b32_e32 v30, 16, v30
	v_pk_add_f32 v[36:37], v[38:39], v[36:37] op_sel_hi:[0,1]
	v_pk_fma_f32 v[36:37], v[30:31], v[30:31], v[36:37]
	v_mul_f32_e32 v38, v31, v31
	v_pk_add_f32 v[36:37], v[38:39], v[36:37] op_sel_hi:[0,1]
	v_pk_fma_f32 v[36:37], v[40:41], v[40:41], v[36:37]
	v_mul_f32_e32 v38, v41, v41
	s_waitcnt vmcnt(0)
	v_and_b32_e32 v27, 0xffff0000, v33
	v_lshlrev_b32_e32 v26, 16, v33
	v_and_b32_e32 v33, 0xffff0000, v32
	v_lshlrev_b32_e32 v32, 16, v32
	v_pk_add_f32 v[36:37], v[38:39], v[36:37] op_sel_hi:[0,1]
	v_pk_fma_f32 v[36:37], v[32:33], v[32:33], v[36:37]
	v_mul_f32_e32 v38, v33, v33
	v_pk_add_f32 v[36:37], v[38:39], v[36:37] op_sel_hi:[0,1]
	v_pk_fma_f32 v[36:37], v[26:27], v[26:27], v[36:37]
	v_mul_f32_e32 v38, v27, v27
	v_and_b32_e32 v25, 0xffff0000, v35
	v_lshlrev_b32_e32 v24, 16, v35
	v_and_b32_e32 v35, 0xffff0000, v34
	v_lshlrev_b32_e32 v34, 16, v34
	v_pk_add_f32 v[36:37], v[38:39], v[36:37] op_sel_hi:[0,1]
	v_pk_fma_f32 v[36:37], v[34:35], v[34:35], v[36:37]
	v_mul_f32_e32 v38, v35, v35
	v_pk_add_f32 v[36:37], v[38:39], v[36:37] op_sel_hi:[0,1]
	v_pk_fma_f32 v[36:37], v[24:25], v[24:25], v[36:37]
	v_mul_f32_e32 v38, v25, v25
	v_pk_add_f32 v[36:37], v[38:39], v[36:37] op_sel_hi:[0,1]
	v_mov_b32_e32 v37, v36
	s_nop 1
	v_permlane32_swap_b32_e32 v36, v37
	v_add_f32_e32 v36, v36, v37
	v_fmamk_f32 v36, v36, 0x3d000000, v196
	v_cmp_gt_f32_e64 s[46:47], s35, v36
	v_mul_f32_e32 v37, 0x4b800000, v36
	s_nop 0
	v_cndmask_b32_e64 v36, v36, v37, s[46:47]
	v_rsq_f32_e32 v36, v36
	s_nop 0
	v_mul_f32_e32 v37, 0x45800000, v36
	v_cndmask_b32_e64 v48, v36, v37, s[46:47]
	v_pk_mul_f32 v[36:37], v[16:17], v[48:49] op_sel_hi:[1,0]
	v_pk_mul_f32 v[44:45], v[20:21], v[48:49] op_sel_hi:[1,0]
	v_pk_mul_f32 v[38:39], v[36:37], v[28:29]
	v_pk_mul_f32 v[36:37], v[44:45], v[30:31]
	v_pk_mul_f32 v[28:29], v[18:19], v[48:49] op_sel_hi:[1,0]
	v_pk_mul_f32 v[30:31], v[22:23], v[48:49] op_sel_hi:[1,0]
	v_pk_mul_f32 v[44:45], v[28:29], v[42:43]
	v_pk_mul_f32 v[40:41], v[30:31], v[40:41]
	v_pk_mul_f32 v[28:29], v[8:9], v[48:49] op_sel_hi:[1,0]
	v_pk_mul_f32 v[30:31], v[12:13], v[48:49] op_sel_hi:[1,0]
	v_pk_mul_f32 v[46:47], v[28:29], v[32:33]
	v_pk_mul_f32 v[42:43], v[30:31], v[34:35]
	v_pk_mul_f32 v[28:29], v[10:11], v[48:49] op_sel_hi:[1,0]
	v_pk_mul_f32 v[30:31], v[14:15], v[48:49] op_sel_hi:[1,0]
	v_pk_mul_f32 v[50:51], v[28:29], v[26:27]
	v_pk_mul_f32 v[48:49], v[30:31], v[24:25]
	s_and_saveexec_b64 s[46:47], vcc
	s_cbranch_execz .LBB0_637
	v_mov_b64_e32 v[28:29], v[118:119]
	v_mov_b64_e32 v[30:31], v[120:121]
	v_mov_b64_e32 v[62:63], v[122:123]
	v_mov_b64_e32 v[64:65], v[124:125]
	v_mov_b64_e32 v[66:67], v[126:127]
	v_mov_b64_e32 v[68:69], v[128:129]
	v_mov_b64_e32 v[60:61], v[130:131]
	v_mov_b64_e32 v[24:25], v[132:133]
	v_mov_b64_e32 v[26:27], v[134:135]
	v_mov_b64_e32 v[32:33], v[136:137]
	v_mov_b64_e32 v[34:35], v[138:139]
	v_mov_b64_e32 v[70:71], v[140:141]
	v_mov_b64_e32 v[72:73], v[142:143]
	v_mov_b64_e32 v[74:75], v[144:145]
	v_mov_b64_e32 v[76:77], v[146:147]
	v_mov_b32_e32 v78, v38
	v_mov_b32_e32 v80, v38
	v_mov_b32_e32 v79, v39
	v_mov_b32_e32 v81, v39
	v_permlane32_swap_b32_e32 v78, v80
	s_nop 0
	v_permlane32_swap_b32_e32 v79, v81
	v_cndmask_b32_e64 v79, v79, v81, s[42:43]
	v_cndmask_b32_e64 v78, v78, v80, s[42:43]
	v_mov_b32_e32 v82, v46
	v_mov_b32_e32 v83, v46
	v_mov_b32_e32 v84, v47
	v_mov_b32_e32 v85, v47
	v_permlane32_swap_b32_e32 v82, v83
	s_nop 0
	v_permlane32_swap_b32_e32 v84, v85
	s_waitcnt vmcnt(5)
	v_mov_b32_e32 v81, v68
	v_mov_b32_e32 v68, v67
	v_mov_b32_e32 v80, v66
	v_pk_mul_f32 v[66:67], v[68:69], v[78:79]
	s_waitcnt vmcnt(0)
	v_mov_b32_e32 v69, v76
	v_cndmask_b32_e64 v67, v67, -v67, s[42:43]
	v_cndmask_b32_e64 v66, v66, -v66, s[42:43]
	v_pk_fma_f32 v[38:39], v[38:39], v[80:81], v[66:67]
	v_cndmask_b32_e64 v67, v84, v85, s[42:43]
	v_cndmask_b32_e64 v66, v82, v83, s[42:43]
	v_mov_b32_e32 v76, v75
	v_pk_mul_f32 v[66:67], v[76:77], v[66:67]
	v_mov_b32_e32 v68, v74
	v_cndmask_b32_e64 v67, v67, -v67, s[42:43]
	v_cndmask_b32_e64 v66, v66, -v66, s[42:43]
	v_pk_fma_f32 v[46:47], v[46:47], v[68:69], v[66:67]
	v_mov_b32_e32 v66, v44
	v_mov_b32_e32 v68, v44
	v_mov_b32_e32 v67, v45
	v_mov_b32_e32 v69, v45
	v_permlane32_swap_b32_e32 v66, v68
	s_nop 0
	v_permlane32_swap_b32_e32 v67, v69
	v_cndmask_b32_e64 v67, v67, v69, s[42:43]
	v_cndmask_b32_e64 v66, v66, v68, s[42:43]
	v_mov_b32_e32 v69, v64
	v_mov_b32_e32 v64, v63
	v_mov_b32_e32 v74, v50
	v_mov_b32_e32 v75, v50
	v_mov_b32_e32 v76, v51
	v_mov_b32_e32 v77, v51
	v_mov_b32_e32 v68, v62
	v_pk_mul_f32 v[62:63], v[64:65], v[66:67]
	v_permlane32_swap_b32_e32 v74, v75
	v_permlane32_swap_b32_e32 v76, v77
	v_cndmask_b32_e64 v63, v63, -v63, s[42:43]
	v_cndmask_b32_e64 v62, v62, -v62, s[42:43]
	v_pk_fma_f32 v[44:45], v[44:45], v[68:69], v[62:63]
	v_cndmask_b32_e64 v63, v76, v77, s[42:43]
	v_cndmask_b32_e64 v62, v74, v75, s[42:43]
	v_mov_b32_e32 v65, v72
	v_mov_b32_e32 v72, v71
	v_pk_mul_f32 v[62:63], v[72:73], v[62:63]
	v_mov_b32_e32 v64, v70
	v_cndmask_b32_e64 v63, v63, -v63, s[42:43]
	v_cndmask_b32_e64 v62, v62, -v62, s[42:43]
	v_pk_fma_f32 v[50:51], v[50:51], v[64:65], v[62:63]
	v_mov_b32_e32 v62, v36
	v_mov_b32_e32 v64, v36
	v_mov_b32_e32 v63, v37
	v_mov_b32_e32 v65, v37
	v_permlane32_swap_b32_e32 v62, v64
	s_nop 0
	v_permlane32_swap_b32_e32 v63, v65
	v_cndmask_b32_e64 v63, v63, v65, s[42:43]
	v_cndmask_b32_e64 v62, v62, v64, s[42:43]
	v_mov_b32_e32 v65, v30
	v_mov_b32_e32 v30, v29
	v_mov_b32_e32 v66, v42
	v_mov_b32_e32 v67, v42
	v_mov_b32_e32 v68, v43
	v_mov_b32_e32 v69, v43
	v_mov_b32_e32 v64, v28
	v_pk_mul_f32 v[28:29], v[30:31], v[62:63]
	v_permlane32_swap_b32_e32 v66, v67
	v_permlane32_swap_b32_e32 v68, v69
	v_cndmask_b32_e64 v29, v29, -v29, s[42:43]
	v_cndmask_b32_e64 v28, v28, -v28, s[42:43]
	v_pk_fma_f32 v[36:37], v[36:37], v[64:65], v[28:29]
	v_cndmask_b32_e64 v29, v68, v69, s[42:43]
	v_cndmask_b32_e64 v28, v66, v67, s[42:43]
	v_mov_b32_e32 v31, v34
	v_mov_b32_e32 v34, v33
	v_pk_mul_f32 v[28:29], v[34:35], v[28:29]
	v_mov_b32_e32 v30, v32
	v_cndmask_b32_e64 v29, v29, -v29, s[42:43]
	v_cndmask_b32_e64 v28, v28, -v28, s[42:43]
	v_pk_fma_f32 v[42:43], v[42:43], v[30:31], v[28:29]
	v_mov_b64_e32 v[28:29], v[148:149]
	v_mov_b32_e32 v30, v40
	v_mov_b32_e32 v32, v40
	v_mov_b32_e32 v31, v41
	v_mov_b32_e32 v33, v41
	v_permlane32_swap_b32_e32 v30, v32
	s_nop 0
	v_permlane32_swap_b32_e32 v31, v33
	v_cndmask_b32_e64 v31, v31, v33, s[42:43]
	v_cndmask_b32_e64 v30, v30, v32, s[42:43]
	v_mov_b32_e32 v34, v48
	v_mov_b32_e32 v35, v48
	v_mov_b32_e32 v62, v49
	v_mov_b32_e32 v63, v49
	v_permlane32_swap_b32_e32 v34, v35
	s_nop 0
	v_permlane32_swap_b32_e32 v62, v63
	v_mov_b32_e32 v32, v60
	s_waitcnt vmcnt(0)
	v_mov_b32_e32 v33, v28
	v_mov_b32_e32 v28, v61
	v_pk_mul_f32 v[28:29], v[28:29], v[30:31]
	v_mov_b32_e32 v31, v26
	v_cndmask_b32_e64 v29, v29, -v29, s[42:43]
	v_cndmask_b32_e64 v28, v28, -v28, s[42:43]
	v_pk_fma_f32 v[40:41], v[40:41], v[32:33], v[28:29]
	v_cndmask_b32_e64 v29, v62, v63, s[42:43]
	v_cndmask_b32_e64 v28, v34, v35, s[42:43]
	v_mov_b32_e32 v26, v25
	v_mov_b32_e32 v30, v24
	v_pk_mul_f32 v[24:25], v[26:27], v[28:29]
	s_nop 0
	v_cndmask_b32_e64 v25, v25, -v25, s[42:43]
	v_cndmask_b32_e64 v24, v24, -v24, s[42:43]
	v_pk_fma_f32 v[48:49], v[48:49], v[30:31], v[24:25]
.LBB0_637:
	s_or_b64 exec, exec, s[46:47]
	s_and_saveexec_b64 s[98:99], vcc
	global_load_dwordx4 v[118:121], v[56:57], off offset:32
	global_load_dwordx4 v[122:125], v[56:57], off offset:16
	global_load_dwordx4 v[126:129], v[56:57], off
	global_load_dwordx2 v[130:131], v[56:57], off offset:48
	global_load_dwordx4 v[132:135], v[54:55], off offset:48
	global_load_dwordx4 v[136:139], v[54:55], off offset:32
	global_load_dwordx4 v[140:143], v[54:55], off offset:16
	global_load_dwordx4 v[144:147], v[54:55], off
	global_load_dwordx2 v[148:149], v[52:53], off
	s_mov_b64 exec, s[98:99]
	v_mov_b64_e32 v[24:25], v[152:153]
	v_mov_b64_e32 v[26:27], v[154:155]
	v_mov_b64_e32 v[28:29], v[156:157]
	v_mov_b64_e32 v[30:31], v[158:159]
	v_and_b32_e32 v61, 0xffff0000, v27
	v_and_b32_e32 v33, 0xffff0000, v31
	v_lshlrev_b32_e32 v32, 16, v31
	v_and_b32_e32 v35, 0xffff0000, v30
	v_lshlrev_b32_e32 v34, 16, v30
	v_and_b32_e32 v59, 0xffff0000, v29
	v_lshlrev_b32_e32 v58, 16, v29
	v_and_b32_e32 v31, 0xffff0000, v28
	v_lshlrev_b32_e32 v30, 16, v28
	v_and_b32_e32 v29, 0xffff0000, v25
	v_lshlrev_b32_e32 v28, 16, v25
	v_and_b32_e32 v25, 0xffff0000, v24
	v_lshlrev_b32_e32 v24, 16, v24
	v_mul_f32_e32 v62, v25, v25
	v_pk_fma_f32 v[62:63], v[24:25], v[24:25], v[62:63] op_sel_hi:[1,1,0]
	v_mul_f32_e32 v64, v29, v29
	v_pk_fma_f32 v[62:63], v[28:29], v[28:29], v[62:63]
	v_lshlrev_b32_e32 v60, 16, v27
	v_and_b32_e32 v27, 0xffff0000, v26
	v_lshlrev_b32_e32 v26, 16, v26
	v_pk_add_f32 v[62:63], v[64:65], v[62:63] op_sel_hi:[0,1]
	v_pk_fma_f32 v[62:63], v[26:27], v[26:27], v[62:63]
	v_mul_f32_e32 v64, v27, v27
	v_pk_add_f32 v[62:63], v[64:65], v[62:63] op_sel_hi:[0,1]
	v_pk_fma_f32 v[62:63], v[60:61], v[60:61], v[62:63]
	v_mul_f32_e32 v64, v61, v61
	v_pk_add_f32 v[62:63], v[64:65], v[62:63] op_sel_hi:[0,1]
	v_pk_fma_f32 v[62:63], v[30:31], v[30:31], v[62:63]
	v_mul_f32_e32 v64, v31, v31
	v_pk_add_f32 v[62:63], v[64:65], v[62:63] op_sel_hi:[0,1]
	v_pk_fma_f32 v[62:63], v[58:59], v[58:59], v[62:63]
	v_mul_f32_e32 v64, v59, v59
	v_pk_add_f32 v[62:63], v[64:65], v[62:63] op_sel_hi:[0,1]
	v_pk_fma_f32 v[62:63], v[34:35], v[34:35], v[62:63]
	v_mul_f32_e32 v64, v35, v35
	v_pk_add_f32 v[62:63], v[64:65], v[62:63] op_sel_hi:[0,1]
	v_pk_fma_f32 v[62:63], v[32:33], v[32:33], v[62:63]
	v_mul_f32_e32 v64, v33, v33
	v_pk_add_f32 v[62:63], v[64:65], v[62:63] op_sel_hi:[0,1]
	v_mov_b32_e32 v63, v62
	s_nop 1
	v_permlane32_swap_b32_e32 v62, v63
	v_add_f32_e32 v62, v62, v63
	v_fmamk_f32 v62, v62, 0x3d000000, v196
	v_cmp_gt_f32_e64 s[46:47], s35, v62
	v_mul_f32_e32 v63, 0x4b800000, v62
	s_nop 0
	v_cndmask_b32_e64 v62, v62, v63, s[46:47]
	v_rsq_f32_e32 v62, v62
	s_nop 0
	v_mul_f32_e32 v63, 0x45800000, v62
	v_cndmask_b32_e64 v62, v62, v63, s[46:47]
	v_pk_mul_f32 v[16:17], v[16:17], v[62:63] op_sel_hi:[1,0]
	v_pk_mul_f32 v[8:9], v[8:9], v[62:63] op_sel_hi:[1,0]
	v_pk_mul_f32 v[20:21], v[20:21], v[62:63] op_sel_hi:[1,0]
	v_pk_mul_f32 v[24:25], v[16:17], v[24:25]
	v_pk_mul_f32 v[16:17], v[18:19], v[62:63] op_sel_hi:[1,0]
	v_pk_mul_f32 v[18:19], v[22:23], v[62:63] op_sel_hi:[1,0]
	v_pk_mul_f32 v[12:13], v[12:13], v[62:63] op_sel_hi:[1,0]
	v_pk_mul_f32 v[30:31], v[8:9], v[30:31]
	v_pk_mul_f32 v[8:9], v[10:11], v[62:63] op_sel_hi:[1,0]
	v_pk_mul_f32 v[10:11], v[14:15], v[62:63] op_sel_hi:[1,0]
	v_pk_mul_f32 v[20:21], v[20:21], v[26:27]
	v_pk_mul_f32 v[28:29], v[16:17], v[28:29]
	v_pk_mul_f32 v[22:23], v[18:19], v[60:61]
	v_pk_mul_f32 v[26:27], v[12:13], v[34:35]
	v_pk_mul_f32 v[34:35], v[8:9], v[58:59]
	v_pk_mul_f32 v[32:33], v[10:11], v[32:33]
	s_and_saveexec_b64 s[46:47], vcc
	s_cbranch_execz .LBB0_639
	s_nop 0
	s_nop 0
	v_mov_b32_e32 v54, v24
	v_mov_b32_e32 v74, v24
	v_mov_b32_e32 v55, v25
	v_mov_b32_e32 v75, v25
	v_permlane32_swap_b32_e32 v54, v74
	s_nop 0
	v_permlane32_swap_b32_e32 v55, v75
	v_cndmask_b32_e64 v55, v55, v75, s[42:43]
	v_cndmask_b32_e64 v54, v54, v74, s[42:43]
	v_mov_b32_e32 v76, v30
	v_mov_b32_e32 v77, v30
	v_mov_b32_e32 v78, v31
	v_mov_b32_e32 v79, v31
	v_permlane32_swap_b32_e32 v76, v77
	s_nop 0
	v_permlane32_swap_b32_e32 v78, v79
	s_waitcnt vmcnt(0)
	v_mov_b64_e32 v[12:13], v[118:119]
	v_mov_b64_e32 v[14:15], v[120:121]
	v_mov_b64_e32 v[58:59], v[122:123]
	v_mov_b64_e32 v[60:61], v[124:125]
	v_mov_b64_e32 v[62:63], v[126:127]
	v_mov_b64_e32 v[64:65], v[128:129]
	v_mov_b64_e32 v[56:57], v[130:131]
	v_mov_b64_e32 v[8:9], v[132:133]
	v_mov_b64_e32 v[10:11], v[134:135]
	v_mov_b64_e32 v[16:17], v[136:137]
	v_mov_b64_e32 v[18:19], v[138:139]
	v_mov_b64_e32 v[66:67], v[140:141]
	v_mov_b64_e32 v[68:69], v[142:143]
	v_mov_b64_e32 v[70:71], v[144:145]
	v_mov_b64_e32 v[72:73], v[146:147]
	v_mov_b32_e32 v75, v64
	v_mov_b32_e32 v64, v63
	v_pk_mul_f32 v[54:55], v[64:65], v[54:55]
	v_mov_b32_e32 v74, v62
	v_cndmask_b32_e64 v55, v55, -v55, s[42:43]
	v_cndmask_b32_e64 v54, v54, -v54, s[42:43]
	v_pk_fma_f32 v[24:25], v[24:25], v[74:75], v[54:55]
	v_cndmask_b32_e64 v55, v78, v79, s[42:43]
	v_cndmask_b32_e64 v54, v76, v77, s[42:43]
	s_waitcnt vmcnt(0)
	v_mov_b32_e32 v63, v72
	v_mov_b32_e32 v72, v71
	v_pk_mul_f32 v[54:55], v[72:73], v[54:55]
	v_mov_b32_e32 v62, v70
	v_cndmask_b32_e64 v55, v55, -v55, s[42:43]
	v_cndmask_b32_e64 v54, v54, -v54, s[42:43]
	v_pk_fma_f32 v[30:31], v[30:31], v[62:63], v[54:55]
	v_mov_b32_e32 v54, v28
	v_mov_b32_e32 v62, v28
	v_mov_b32_e32 v55, v29
	v_mov_b32_e32 v63, v29
	v_permlane32_swap_b32_e32 v54, v62
	s_nop 0
	v_permlane32_swap_b32_e32 v55, v63
	v_cndmask_b32_e64 v55, v55, v63, s[42:43]
	v_cndmask_b32_e64 v54, v54, v62, s[42:43]
	v_mov_b32_e32 v63, v60
	v_mov_b32_e32 v60, v59
	v_mov_b32_e32 v64, v34
	v_mov_b32_e32 v65, v34
	v_mov_b32_e32 v70, v35
	v_mov_b32_e32 v71, v35
	v_pk_mul_f32 v[54:55], v[60:61], v[54:55]
	v_permlane32_swap_b32_e32 v64, v65
	v_permlane32_swap_b32_e32 v70, v71
	v_mov_b32_e32 v62, v58
	v_cndmask_b32_e64 v55, v55, -v55, s[42:43]
	v_cndmask_b32_e64 v54, v54, -v54, s[42:43]
	v_pk_fma_f32 v[28:29], v[28:29], v[62:63], v[54:55]
	v_cndmask_b32_e64 v55, v70, v71, s[42:43]
	v_cndmask_b32_e64 v54, v64, v65, s[42:43]
	v_mov_b32_e32 v59, v68
	v_mov_b32_e32 v68, v67
	v_pk_mul_f32 v[54:55], v[68:69], v[54:55]
	v_mov_b32_e32 v58, v66
	v_cndmask_b32_e64 v55, v55, -v55, s[42:43]
	v_cndmask_b32_e64 v54, v54, -v54, s[42:43]
	v_pk_fma_f32 v[34:35], v[34:35], v[58:59], v[54:55]
	v_mov_b32_e32 v54, v20
	v_mov_b32_e32 v58, v20
	v_mov_b32_e32 v55, v21
	v_mov_b32_e32 v59, v21
	v_permlane32_swap_b32_e32 v54, v58
	s_nop 0
	v_permlane32_swap_b32_e32 v55, v59
	v_cndmask_b32_e64 v55, v55, v59, s[42:43]
	v_cndmask_b32_e64 v54, v54, v58, s[42:43]
	v_mov_b32_e32 v59, v14
	v_mov_b32_e32 v14, v13
	v_mov_b32_e32 v60, v26
	v_mov_b32_e32 v61, v26
	v_mov_b32_e32 v62, v27
	v_mov_b32_e32 v63, v27
	v_mov_b32_e32 v58, v12
	v_pk_mul_f32 v[12:13], v[14:15], v[54:55]
	v_permlane32_swap_b32_e32 v60, v61
	v_permlane32_swap_b32_e32 v62, v63
	v_cndmask_b32_e64 v13, v13, -v13, s[42:43]
	v_cndmask_b32_e64 v12, v12, -v12, s[42:43]
	v_pk_fma_f32 v[20:21], v[20:21], v[58:59], v[12:13]
	v_cndmask_b32_e64 v13, v62, v63, s[42:43]
	v_cndmask_b32_e64 v12, v60, v61, s[42:43]
	v_mov_b32_e32 v15, v18
	v_mov_b32_e32 v18, v17
	v_pk_mul_f32 v[12:13], v[18:19], v[12:13]
	v_mov_b32_e32 v14, v16
	v_cndmask_b32_e64 v13, v13, -v13, s[42:43]
	v_cndmask_b32_e64 v12, v12, -v12, s[42:43]
	v_pk_fma_f32 v[26:27], v[26:27], v[14:15], v[12:13]
	v_mov_b64_e32 v[12:13], v[148:149]
	v_mov_b32_e32 v14, v22
	v_mov_b32_e32 v16, v22
	v_mov_b32_e32 v15, v23
	v_mov_b32_e32 v17, v23
	v_permlane32_swap_b32_e32 v14, v16
	s_nop 0
	v_permlane32_swap_b32_e32 v15, v17
	v_cndmask_b32_e64 v15, v15, v17, s[42:43]
	v_cndmask_b32_e64 v14, v14, v16, s[42:43]
	v_mov_b32_e32 v18, v32
	v_mov_b32_e32 v19, v32
	v_mov_b32_e32 v52, v33
	v_mov_b32_e32 v53, v33
	v_permlane32_swap_b32_e32 v18, v19
	s_nop 0
	v_permlane32_swap_b32_e32 v52, v53
	v_mov_b32_e32 v16, v56
	s_waitcnt vmcnt(0)
	v_mov_b32_e32 v17, v12
	v_mov_b32_e32 v12, v57
	v_pk_mul_f32 v[12:13], v[12:13], v[14:15]
	v_mov_b32_e32 v15, v10
	v_cndmask_b32_e64 v13, v13, -v13, s[42:43]
	v_cndmask_b32_e64 v12, v12, -v12, s[42:43]
	v_pk_fma_f32 v[22:23], v[22:23], v[16:17], v[12:13]
	v_cndmask_b32_e64 v13, v52, v53, s[42:43]
	v_cndmask_b32_e64 v12, v18, v19, s[42:43]
	v_mov_b32_e32 v10, v9
	v_mov_b32_e32 v14, v8
	v_pk_mul_f32 v[8:9], v[10:11], v[12:13]
	s_nop 0
	v_cndmask_b32_e64 v9, v9, -v9, s[42:43]
	v_cndmask_b32_e64 v8, v8, -v8, s[42:43]
	v_pk_fma_f32 v[32:33], v[32:33], v[14:15], v[8:9]
